# de-serialisation in the attention pick prologue: fq load issued right after the schedule decode (in front of the pick barrier) instead of behind the key-bias copy loop; on top of v60
# speedup vs baseline: 1.0042x; 1.0005x over previous
.LBB0_1689:
	s_lshl_b32 s9, s47, 8
	s_sub_i32 s30, s9, s95
	s_and_b32 s8, s47, 1
	s_addk_i32 s30, 0xff
	s_add_i32 s9, s9, s95
	s_cmp_eq_u32 s8, 0
	s_cselect_b32 s8, s9, s30
	s_lshl_b32 s8, s8, 2
	s_add_i32 s8, s8, 0
	s_add_i32 s8, s8, 0x1d100
	v_mov_b32_e32 v2, s8
	ds_read_b32 v2, v2
	s_waitcnt lgkmcnt(0)
	v_readfirstlane_b32 s8, v2
	s_cmp_eq_u32 s8, 0
	s_cbranch_scc1 .LBB0_1688
	s_and_b32 s30, s8, 0x3ff
	s_lshl_b32 s9, s30, 2
	s_add_i32 s9, s9, 0
	s_add_i32 s9, s9, 0x1f100
	v_mov_b32_e32 v2, s9
	ds_read_b32 v2, v2
	s_and_b32 s42, s8, 31
	s_lshl_b32 s9, s42, 2
	s_or_b32 s9, s9, 1
	s_bfe_u32 s43, s8, 0x2000a
	s_waitcnt lgkmcnt(0)
	v_readfirstlane_b32 s44, v2
	s_and_b32 s34, s44, 0xff
	s_sub_i32 s9, s9, s34
	s_ashr_i32 s9, s9, 1
	s_ashr_i32 s49, s8, 12
	s_and_b32 s9, s9, -2
	s_cmp_eq_u32 s43, 2
	s_cselect_b32 s41, s9, 0
	s_lshl_b32 s40, s49, 6
	s_add_i32 s41, s41, s34
	v_mov_b32_e32 v246, s30
	v_lshrrev_b32_e32 v246, 5, v246
	v_mul_u32_u24_e32 v246, 0x8100, v246
	v_lshl_add_u32 v246, s42, 10, v246
	v_lshl_add_u32 v246, v0, 2, v246
	global_load_dword v247, v246, s[54:55] offset:256
	v_cmp_gt_i32_e32 vcc, s40, v252
	s_barrier
	s_and_saveexec_b64 s[34:35], vcc
	s_cbranch_execz .LBB0_1693
	s_lshl_b32 s38, s41, 6
	s_ashr_i32 s39, s38, 31
	s_cmp_lg_u32 s43, 1
	s_cselect_b64 s[36:37], -1, 0
	s_bfe_u32 s8, s8, 0x50005
	s_lshl_b32 s45, s9, 6
	s_mul_i32 s48, s8, 0x8100
	s_lshl_b64 s[8:9], s[38:39], 2
	s_add_u32 s8, s48, s8
	s_addc_u32 s9, 0, s9
	v_lshl_add_u64 v[2:3], v[210:211], 0, s[8:9]
	s_mov_b64 s[38:39], 0
	v_mov_b32_e32 v4, v236
	v_mov_b32_e32 v5, v252

.LBB0_1693:
	s_or_b64 exec, exec, s[34:35]
	s_lshr_b32 s34, s30, 5
	s_and_saveexec_b64 s[8:9], s[6:7]
	s_cbranch_execz .LBB0_1695
	s_waitcnt vmcnt(0)
	ds_write_b32 v230, v247
